# skip the second grid barrier between MoE gate/up and down phases when the deferred-conversion cleanup has nothing left
# speedup vs baseline: 1.0082x; 1.0040x over previous
; static __device__ __forceinline__ void conv_impl(LAS unsigned char* lds, unsigned char* ws, const float* win, const float* wout, const float* wqkv, const float* wao, const float* mg, const float* mu, const float* md, ...
;     ...
;     if (qhead) { deferred = true;
;         if (quota >= 0) { unsigned d = 0u; if (lane == 0) d = __hip_atomic_fetch_add(qhead, (unsigned)quota, __ATOMIC_RELAXED, __HIP_MEMORY_SCOPE_AGENT);
;             it0 = __builtin_amdgcn_readfirstlane((int)d); it_hi = it0 + quota; NGW = 1; }
;         else { const unsigned h = __hip_atomic_load(qhead, __ATOMIC_RELAXED, __HIP_MEMORY_SCOPE_AGENT); it0 = (int)h + gw; }
;         if (it_hi > 6 * HALFM) it_hi = 6 * HALFM; }
;     for (;;) {
;         if (it0 >= it_hi) break;
;         int it = it0; it0 += NGW;
; __global__ void __launch_bounds__(NTHREADS, 2) mk_fwd(Args args) {
;     ...
;     if (IN(9) && IN(10)) { conv_cleanup(F, args, 3 * cv::HALFM); xcd_barrier(bar); }
.LBB0_1900:
	s_or_b64 exec, exec, s[0:1]
	s_waitcnt lgkmcnt(0)
	v_mov_b32_e32 v2, 0x2000
	s_barrier
	global_load_dword v2, v2, s[92:93] sc1
	s_lshl_b32 s0, s3, 3
	s_add_i32 s0, s74, s0
	s_waitcnt vmcnt(0)
	v_readfirstlane_b32 s1, v2
	s_cmp_gt_u32 s1, 0xc2ff
	s_cbranch_scc1 .LBB0_2051
	s_add_i32 s30, s0, s1
	s_cmp_gt_i32 s30, 0xc2ff
	s_cbranch_scc1 .LBB0_1998
	v_readlane_b32 s0, v254, 0
	s_lshl_b32 s31, s0, 3
	s_add_u32 s34, s92, 0x23800000
	s_addc_u32 s35, s93, 0
	s_add_u32 s36, s92, 0x3000000
	s_addc_u32 s37, s93, 0
	s_add_u32 s6, s92, 0x2800000
	s_addc_u32 s7, s93, 0
	s_add_u32 s8, s92, 0x1c00000
	s_addc_u32 s9, s93, 0
	v_lshrrev_b32_e32 v2, 6, v0
	s_movk_i32 s0, 0x4200
	s_add_u32 s10, s92, 0x2600000
	v_mad_u32_u24 v5, v2, s0, 0
	s_addc_u32 s11, s93, 0
	v_lshlrev_b32_e32 v2, 2, v0
	s_add_u32 s12, s92, 0x1400000
	v_lshrrev_b32_e32 v14, 3, v1
	v_and_b32_e32 v4, 28, v2
	v_lshlrev_b32_e32 v2, 3, v0
	s_addc_u32 s13, s93, 0
	v_lshl_add_u32 v6, v4, 2, v5
	v_mul_u32_u24_e32 v7, 0x84, v14
	v_lshrrev_b32_e32 v15, 4, v1
	v_and_b32_e32 v2, 0x78, v2
	v_readlane_b32 s1, v254, 1
	s_add_u32 s14, s92, 0x800000
	v_mov_b32_e32 v3, 0
	v_mul_u32_u24_e32 v8, 0x84, v2
	v_lshlrev_b32_e32 v9, 2, v15
	v_add_u32_e32 v24, v6, v7
	s_mov_b32 s1, 0
	s_addc_u32 s15, s93, 0
	v_add3_u32 v16, v5, v8, v9
	v_or_b32_e32 v17, 4, v15
	v_or_b32_e32 v18, 8, v15
	v_or_b32_e32 v19, 12, v15
	v_or_b32_e32 v20, 16, v15
	v_or_b32_e32 v21, 20, v15
	v_or_b32_e32 v22, 24, v15
	v_or_b32_e32 v23, 28, v15
	s_movk_i32 s2, 0x5500
	s_movk_i32 s33, 0x9ff
	s_mov_b32 s38, 0xffff6a00
	v_lshlrev_b32_e32 v4, 2, v4
	v_mov_b32_e32 v5, v3
	v_add_u32_e32 v25, 0x420, v24
	v_add_u32_e32 v26, 0x428, v24
	v_add_u32_e32 v27, 0x840, v24
	v_add_u32_e32 v28, 0x848, v24
	v_add_u32_e32 v29, 0xc60, v24
	v_add_u32_e32 v30, 0xc68, v24
	v_add_u32_e32 v31, 0x1080, v24
	v_add_u32_e32 v32, 0x1088, v24
	v_add_u32_e32 v33, 0x14a0, v24
	v_add_u32_e32 v34, 0x14a8, v24
	v_add_u32_e32 v35, 0x18c0, v24
	v_add_u32_e32 v36, 0x18c8, v24
	v_add_u32_e32 v37, 0x1ce0, v24
	v_add_u32_e32 v38, 0x1ce8, v24
	v_add_u32_e32 v39, 0x2100, v24
	v_add_u32_e32 v40, 0x2108, v24
	v_add_u32_e32 v41, 0x2520, v24
	v_add_u32_e32 v42, 0x2528, v24
	v_add_u32_e32 v43, 0x2940, v24
	v_add_u32_e32 v44, 0x2948, v24
	v_add_u32_e32 v45, 0x2d60, v24
	v_add_u32_e32 v46, 0x2d68, v24
	v_add_u32_e32 v47, 0x3180, v24
	v_add_u32_e32 v48, 0x3188, v24
	v_add_u32_e32 v49, 0x35a0, v24
	v_add_u32_e32 v50, 0x35a8, v24
	v_add_u32_e32 v51, 0x39c0, v24
	v_add_u32_e32 v52, 0x39c8, v24
	v_add_u32_e32 v53, 0x3de0, v24
	v_add_u32_e32 v54, 0x3de8, v24
	s_mov_b32 s39, 0xc3e00000
	v_mov_b32_e32 v55, 0x43e00000
	s_branch .LBB0_1904
